# speedup vs baseline: 1.0291x; 1.0089x over previous
_Z11prep_kernelPKfS0_S0_PDF16_PfPiS0_S1_:
	s_cmpk_lt_u32 s2, 0xc1
	s_mov_b64 s[4:5], -1
	s_cbranch_scc0 .LBB0_51
	s_cmpk_lg_i32 s2, 0xc0
	s_cbranch_scc0 .LBB0_11
	s_cmp_gt_u32 s2, 63
	s_cbranch_scc0 .LBB0_8
	s_load_dwordx4 s[4:7], s[0:1], 0x0
	s_load_dwordx2 s[28:29], s[0:1], 0x20
	s_sub_u32 s3, s2, 64
	v_readfirstlane_b32 s23, v0
	v_and_b32_e32 v1, 63, v0
	v_lshlrev_b32_e32 v100, 4, v1
	s_lshr_b32 s23, s23, 6
	s_lshr_b32 s27, s3, 1
	s_and_b32 s30, s3, 1
	s_lshl_b32 s8, s27, 12
	s_lshl_b32 s9, s23, 6
	s_add_u32 s8, s8, s9
	s_lshl_b32 s10, s23, 15
	s_lshl_b32 s9, s30, 10
	s_add_u32 s10, s10, s9
	s_waitcnt lgkmcnt(0)
	s_add_u32 s20, s4, s8
	s_addc_u32 s21, s5, 0
	s_add_u32 s24, s6, s10
	s_addc_u32 s25, s7, 0
	global_load_dwordx4 v[34:37], v100, s[24:25]
	global_load_dwordx4 v[38:41], v100, s[24:25] offset:2048
	s_add_u32 s24, s24, 0x1000
	s_addc_u32 s25, s25, 0
	s_load_dwordx8 s[32:39], s[20:21], 0x0
	s_load_dwordx8 s[40:47], s[20:21], 0x200
	s_load_dwordx8 s[48:55], s[20:21], 0x400
	s_load_dwordx8 s[56:63], s[20:21], 0x600
	global_load_dwordx4 v[42:45], v100, s[24:25]
	global_load_dwordx4 v[46:49], v100, s[24:25] offset:2048
	s_add_u32 s24, s24, 0x1000
	s_addc_u32 s25, s25, 0
	s_load_dwordx8 s[64:71], s[20:21], 0x20
	s_load_dwordx8 s[72:79], s[20:21], 0x220
	s_load_dwordx8 s[80:87], s[20:21], 0x420
	s_load_dwordx8 s[88:95], s[20:21], 0x620
	global_load_dwordx4 v[50:53], v100, s[24:25]
	global_load_dwordx4 v[54:57], v100, s[24:25] offset:2048
	s_add_u32 s24, s24, 0x1000
	s_addc_u32 s25, s25, 0
	global_load_dwordx4 v[58:61], v100, s[24:25]
	global_load_dwordx4 v[62:65], v100, s[24:25] offset:2048
	s_add_u32 s24, s24, 0x1000
	s_addc_u32 s25, s25, 0
	global_load_dwordx4 v[66:69], v100, s[24:25]
	global_load_dwordx4 v[70:73], v100, s[24:25] offset:2048
	s_add_u32 s24, s24, 0x1000
	s_addc_u32 s25, s25, 0
	global_load_dwordx4 v[74:77], v100, s[24:25]
	global_load_dwordx4 v[78:81], v100, s[24:25] offset:2048
	s_add_u32 s24, s24, 0x1000
	s_addc_u32 s25, s25, 0
	global_load_dwordx4 v[82:85], v100, s[24:25]
	global_load_dwordx4 v[86:89], v100, s[24:25] offset:2048
	s_add_u32 s24, s24, 0x1000
	s_addc_u32 s25, s25, 0
	global_load_dwordx4 v[90:93], v100, s[24:25]
	global_load_dwordx4 v[94:97], v100, s[24:25] offset:2048
	v_mov_b64_e32 v[2:3], 0
	v_mov_b64_e32 v[4:5], 0
	v_mov_b64_e32 v[6:7], 0
	v_mov_b64_e32 v[8:9], 0
	v_mov_b64_e32 v[10:11], 0
	v_mov_b64_e32 v[12:13], 0
	v_mov_b64_e32 v[14:15], 0
	v_mov_b64_e32 v[16:17], 0
	v_mov_b64_e32 v[18:19], 0
	v_mov_b64_e32 v[20:21], 0
	v_mov_b64_e32 v[22:23], 0
	v_mov_b64_e32 v[24:25], 0
	v_mov_b64_e32 v[26:27], 0
	v_mov_b64_e32 v[28:29], 0
	v_mov_b64_e32 v[30:31], 0
	v_mov_b64_e32 v[32:33], 0
	s_waitcnt lgkmcnt(0)
	s_waitcnt vmcnt(15)
	v_pk_fma_f32 v[2:3], s[32:33], v[34:35], v[2:3] op_sel_hi:[0,1,1]
	v_pk_fma_f32 v[4:5], s[32:33], v[36:37], v[4:5] op_sel_hi:[0,1,1]
	v_pk_fma_f32 v[6:7], s[40:41], v[34:35], v[6:7] op_sel_hi:[0,1,1]
	v_pk_fma_f32 v[8:9], s[40:41], v[36:37], v[8:9] op_sel_hi:[0,1,1]
	v_pk_fma_f32 v[10:11], s[48:49], v[34:35], v[10:11] op_sel_hi:[0,1,1]
	v_pk_fma_f32 v[12:13], s[48:49], v[36:37], v[12:13] op_sel_hi:[0,1,1]
	v_pk_fma_f32 v[14:15], s[56:57], v[34:35], v[14:15] op_sel_hi:[0,1,1]
	v_pk_fma_f32 v[16:17], s[56:57], v[36:37], v[16:17] op_sel_hi:[0,1,1]
	s_waitcnt vmcnt(14)
	v_pk_fma_f32 v[2:3], s[32:33], v[38:39], v[2:3] op_sel:[1,0,0]
	v_pk_fma_f32 v[4:5], s[32:33], v[40:41], v[4:5] op_sel:[1,0,0]
	v_pk_fma_f32 v[6:7], s[40:41], v[38:39], v[6:7] op_sel:[1,0,0]
	v_pk_fma_f32 v[8:9], s[40:41], v[40:41], v[8:9] op_sel:[1,0,0]
	v_pk_fma_f32 v[10:11], s[48:49], v[38:39], v[10:11] op_sel:[1,0,0]
	v_pk_fma_f32 v[12:13], s[48:49], v[40:41], v[12:13] op_sel:[1,0,0]
	v_pk_fma_f32 v[14:15], s[56:57], v[38:39], v[14:15] op_sel:[1,0,0]
	v_pk_fma_f32 v[16:17], s[56:57], v[40:41], v[16:17] op_sel:[1,0,0]
	s_waitcnt vmcnt(13)
	v_pk_fma_f32 v[2:3], s[34:35], v[42:43], v[2:3] op_sel_hi:[0,1,1]
	v_pk_fma_f32 v[4:5], s[34:35], v[44:45], v[4:5] op_sel_hi:[0,1,1]
	v_pk_fma_f32 v[6:7], s[42:43], v[42:43], v[6:7] op_sel_hi:[0,1,1]
	v_pk_fma_f32 v[8:9], s[42:43], v[44:45], v[8:9] op_sel_hi:[0,1,1]
	v_pk_fma_f32 v[10:11], s[50:51], v[42:43], v[10:11] op_sel_hi:[0,1,1]
	v_pk_fma_f32 v[12:13], s[50:51], v[44:45], v[12:13] op_sel_hi:[0,1,1]
	v_pk_fma_f32 v[14:15], s[58:59], v[42:43], v[14:15] op_sel_hi:[0,1,1]
	v_pk_fma_f32 v[16:17], s[58:59], v[44:45], v[16:17] op_sel_hi:[0,1,1]
	s_waitcnt vmcnt(12)
	v_pk_fma_f32 v[2:3], s[34:35], v[46:47], v[2:3] op_sel:[1,0,0]
	v_pk_fma_f32 v[4:5], s[34:35], v[48:49], v[4:5] op_sel:[1,0,0]
	v_pk_fma_f32 v[6:7], s[42:43], v[46:47], v[6:7] op_sel:[1,0,0]
	v_pk_fma_f32 v[8:9], s[42:43], v[48:49], v[8:9] op_sel:[1,0,0]
	v_pk_fma_f32 v[10:11], s[50:51], v[46:47], v[10:11] op_sel:[1,0,0]
	v_pk_fma_f32 v[12:13], s[50:51], v[48:49], v[12:13] op_sel:[1,0,0]
	v_pk_fma_f32 v[14:15], s[58:59], v[46:47], v[14:15] op_sel:[1,0,0]
	v_pk_fma_f32 v[16:17], s[58:59], v[48:49], v[16:17] op_sel:[1,0,0]
	s_waitcnt vmcnt(11)
	v_pk_fma_f32 v[2:3], s[36:37], v[50:51], v[2:3] op_sel_hi:[0,1,1]
	v_pk_fma_f32 v[4:5], s[36:37], v[52:53], v[4:5] op_sel_hi:[0,1,1]
	v_pk_fma_f32 v[6:7], s[44:45], v[50:51], v[6:7] op_sel_hi:[0,1,1]
	v_pk_fma_f32 v[8:9], s[44:45], v[52:53], v[8:9] op_sel_hi:[0,1,1]
	v_pk_fma_f32 v[10:11], s[52:53], v[50:51], v[10:11] op_sel_hi:[0,1,1]
	v_pk_fma_f32 v[12:13], s[52:53], v[52:53], v[12:13] op_sel_hi:[0,1,1]
	v_pk_fma_f32 v[14:15], s[60:61], v[50:51], v[14:15] op_sel_hi:[0,1,1]
	v_pk_fma_f32 v[16:17], s[60:61], v[52:53], v[16:17] op_sel_hi:[0,1,1]
	s_waitcnt vmcnt(10)
	v_pk_fma_f32 v[2:3], s[36:37], v[54:55], v[2:3] op_sel:[1,0,0]
	v_pk_fma_f32 v[4:5], s[36:37], v[56:57], v[4:5] op_sel:[1,0,0]
	v_pk_fma_f32 v[6:7], s[44:45], v[54:55], v[6:7] op_sel:[1,0,0]
	v_pk_fma_f32 v[8:9], s[44:45], v[56:57], v[8:9] op_sel:[1,0,0]
	v_pk_fma_f32 v[10:11], s[52:53], v[54:55], v[10:11] op_sel:[1,0,0]
	v_pk_fma_f32 v[12:13], s[52:53], v[56:57], v[12:13] op_sel:[1,0,0]
	v_pk_fma_f32 v[14:15], s[60:61], v[54:55], v[14:15] op_sel:[1,0,0]
	v_pk_fma_f32 v[16:17], s[60:61], v[56:57], v[16:17] op_sel:[1,0,0]
	s_waitcnt vmcnt(9)
	v_pk_fma_f32 v[2:3], s[38:39], v[58:59], v[2:3] op_sel_hi:[0,1,1]
	v_pk_fma_f32 v[4:5], s[38:39], v[60:61], v[4:5] op_sel_hi:[0,1,1]
	v_pk_fma_f32 v[6:7], s[46:47], v[58:59], v[6:7] op_sel_hi:[0,1,1]
	v_pk_fma_f32 v[8:9], s[46:47], v[60:61], v[8:9] op_sel_hi:[0,1,1]
	v_pk_fma_f32 v[10:11], s[54:55], v[58:59], v[10:11] op_sel_hi:[0,1,1]
	v_pk_fma_f32 v[12:13], s[54:55], v[60:61], v[12:13] op_sel_hi:[0,1,1]
	v_pk_fma_f32 v[14:15], s[62:63], v[58:59], v[14:15] op_sel_hi:[0,1,1]
	v_pk_fma_f32 v[16:17], s[62:63], v[60:61], v[16:17] op_sel_hi:[0,1,1]
	s_waitcnt vmcnt(8)
	v_pk_fma_f32 v[2:3], s[38:39], v[62:63], v[2:3] op_sel:[1,0,0]
	v_pk_fma_f32 v[4:5], s[38:39], v[64:65], v[4:5] op_sel:[1,0,0]
	v_pk_fma_f32 v[6:7], s[46:47], v[62:63], v[6:7] op_sel:[1,0,0]
	v_pk_fma_f32 v[8:9], s[46:47], v[64:65], v[8:9] op_sel:[1,0,0]
	v_pk_fma_f32 v[10:11], s[54:55], v[62:63], v[10:11] op_sel:[1,0,0]
	v_pk_fma_f32 v[12:13], s[54:55], v[64:65], v[12:13] op_sel:[1,0,0]
	v_pk_fma_f32 v[14:15], s[62:63], v[62:63], v[14:15] op_sel:[1,0,0]
	v_pk_fma_f32 v[16:17], s[62:63], v[64:65], v[16:17] op_sel:[1,0,0]
	s_load_dwordx8 s[32:39], s[20:21], 0x800
	s_load_dwordx8 s[40:47], s[20:21], 0xa00
	s_load_dwordx8 s[48:55], s[20:21], 0xc00
	s_load_dwordx8 s[56:63], s[20:21], 0xe00
	s_waitcnt vmcnt(7)
	v_pk_fma_f32 v[2:3], s[64:65], v[66:67], v[2:3] op_sel_hi:[0,1,1]
	v_pk_fma_f32 v[4:5], s[64:65], v[68:69], v[4:5] op_sel_hi:[0,1,1]
	v_pk_fma_f32 v[6:7], s[72:73], v[66:67], v[6:7] op_sel_hi:[0,1,1]
	v_pk_fma_f32 v[8:9], s[72:73], v[68:69], v[8:9] op_sel_hi:[0,1,1]
	v_pk_fma_f32 v[10:11], s[80:81], v[66:67], v[10:11] op_sel_hi:[0,1,1]
	v_pk_fma_f32 v[12:13], s[80:81], v[68:69], v[12:13] op_sel_hi:[0,1,1]
	v_pk_fma_f32 v[14:15], s[88:89], v[66:67], v[14:15] op_sel_hi:[0,1,1]
	v_pk_fma_f32 v[16:17], s[88:89], v[68:69], v[16:17] op_sel_hi:[0,1,1]
	s_waitcnt vmcnt(6)
	v_pk_fma_f32 v[2:3], s[64:65], v[70:71], v[2:3] op_sel:[1,0,0]
	v_pk_fma_f32 v[4:5], s[64:65], v[72:73], v[4:5] op_sel:[1,0,0]
	v_pk_fma_f32 v[6:7], s[72:73], v[70:71], v[6:7] op_sel:[1,0,0]
	v_pk_fma_f32 v[8:9], s[72:73], v[72:73], v[8:9] op_sel:[1,0,0]
	v_pk_fma_f32 v[10:11], s[80:81], v[70:71], v[10:11] op_sel:[1,0,0]
	v_pk_fma_f32 v[12:13], s[80:81], v[72:73], v[12:13] op_sel:[1,0,0]
	v_pk_fma_f32 v[14:15], s[88:89], v[70:71], v[14:15] op_sel:[1,0,0]
	v_pk_fma_f32 v[16:17], s[88:89], v[72:73], v[16:17] op_sel:[1,0,0]
	s_waitcnt vmcnt(5)
	v_pk_fma_f32 v[2:3], s[66:67], v[74:75], v[2:3] op_sel_hi:[0,1,1]
	v_pk_fma_f32 v[4:5], s[66:67], v[76:77], v[4:5] op_sel_hi:[0,1,1]
	v_pk_fma_f32 v[6:7], s[74:75], v[74:75], v[6:7] op_sel_hi:[0,1,1]
	v_pk_fma_f32 v[8:9], s[74:75], v[76:77], v[8:9] op_sel_hi:[0,1,1]
	v_pk_fma_f32 v[10:11], s[82:83], v[74:75], v[10:11] op_sel_hi:[0,1,1]
	v_pk_fma_f32 v[12:13], s[82:83], v[76:77], v[12:13] op_sel_hi:[0,1,1]
	v_pk_fma_f32 v[14:15], s[90:91], v[74:75], v[14:15] op_sel_hi:[0,1,1]
	v_pk_fma_f32 v[16:17], s[90:91], v[76:77], v[16:17] op_sel_hi:[0,1,1]
	s_waitcnt vmcnt(4)
	v_pk_fma_f32 v[2:3], s[66:67], v[78:79], v[2:3] op_sel:[1,0,0]
	v_pk_fma_f32 v[4:5], s[66:67], v[80:81], v[4:5] op_sel:[1,0,0]
	v_pk_fma_f32 v[6:7], s[74:75], v[78:79], v[6:7] op_sel:[1,0,0]
	v_pk_fma_f32 v[8:9], s[74:75], v[80:81], v[8:9] op_sel:[1,0,0]
	v_pk_fma_f32 v[10:11], s[82:83], v[78:79], v[10:11] op_sel:[1,0,0]
	v_pk_fma_f32 v[12:13], s[82:83], v[80:81], v[12:13] op_sel:[1,0,0]
	v_pk_fma_f32 v[14:15], s[90:91], v[78:79], v[14:15] op_sel:[1,0,0]
	v_pk_fma_f32 v[16:17], s[90:91], v[80:81], v[16:17] op_sel:[1,0,0]
	s_waitcnt vmcnt(3)
	v_pk_fma_f32 v[2:3], s[68:69], v[82:83], v[2:3] op_sel_hi:[0,1,1]
	v_pk_fma_f32 v[4:5], s[68:69], v[84:85], v[4:5] op_sel_hi:[0,1,1]
	v_pk_fma_f32 v[6:7], s[76:77], v[82:83], v[6:7] op_sel_hi:[0,1,1]
	v_pk_fma_f32 v[8:9], s[76:77], v[84:85], v[8:9] op_sel_hi:[0,1,1]
	v_pk_fma_f32 v[10:11], s[84:85], v[82:83], v[10:11] op_sel_hi:[0,1,1]
	v_pk_fma_f32 v[12:13], s[84:85], v[84:85], v[12:13] op_sel_hi:[0,1,1]
	v_pk_fma_f32 v[14:15], s[92:93], v[82:83], v[14:15] op_sel_hi:[0,1,1]
	v_pk_fma_f32 v[16:17], s[92:93], v[84:85], v[16:17] op_sel_hi:[0,1,1]
	s_waitcnt vmcnt(2)
	v_pk_fma_f32 v[2:3], s[68:69], v[86:87], v[2:3] op_sel:[1,0,0]
	v_pk_fma_f32 v[4:5], s[68:69], v[88:89], v[4:5] op_sel:[1,0,0]
	v_pk_fma_f32 v[6:7], s[76:77], v[86:87], v[6:7] op_sel:[1,0,0]
	v_pk_fma_f32 v[8:9], s[76:77], v[88:89], v[8:9] op_sel:[1,0,0]
	v_pk_fma_f32 v[10:11], s[84:85], v[86:87], v[10:11] op_sel:[1,0,0]
	v_pk_fma_f32 v[12:13], s[84:85], v[88:89], v[12:13] op_sel:[1,0,0]
	v_pk_fma_f32 v[14:15], s[92:93], v[86:87], v[14:15] op_sel:[1,0,0]
	v_pk_fma_f32 v[16:17], s[92:93], v[88:89], v[16:17] op_sel:[1,0,0]
	s_waitcnt vmcnt(1)
	v_pk_fma_f32 v[2:3], s[70:71], v[90:91], v[2:3] op_sel_hi:[0,1,1]
	v_pk_fma_f32 v[4:5], s[70:71], v[92:93], v[4:5] op_sel_hi:[0,1,1]
	v_pk_fma_f32 v[6:7], s[78:79], v[90:91], v[6:7] op_sel_hi:[0,1,1]
	v_pk_fma_f32 v[8:9], s[78:79], v[92:93], v[8:9] op_sel_hi:[0,1,1]
	v_pk_fma_f32 v[10:11], s[86:87], v[90:91], v[10:11] op_sel_hi:[0,1,1]
	v_pk_fma_f32 v[12:13], s[86:87], v[92:93], v[12:13] op_sel_hi:[0,1,1]
	v_pk_fma_f32 v[14:15], s[94:95], v[90:91], v[14:15] op_sel_hi:[0,1,1]
	v_pk_fma_f32 v[16:17], s[94:95], v[92:93], v[16:17] op_sel_hi:[0,1,1]
	s_waitcnt vmcnt(0)
	v_pk_fma_f32 v[2:3], s[70:71], v[94:95], v[2:3] op_sel:[1,0,0]
	v_pk_fma_f32 v[4:5], s[70:71], v[96:97], v[4:5] op_sel:[1,0,0]
	v_pk_fma_f32 v[6:7], s[78:79], v[94:95], v[6:7] op_sel:[1,0,0]
	v_pk_fma_f32 v[8:9], s[78:79], v[96:97], v[8:9] op_sel:[1,0,0]
	v_pk_fma_f32 v[10:11], s[86:87], v[94:95], v[10:11] op_sel:[1,0,0]
	v_pk_fma_f32 v[12:13], s[86:87], v[96:97], v[12:13] op_sel:[1,0,0]
	v_pk_fma_f32 v[14:15], s[94:95], v[94:95], v[14:15] op_sel:[1,0,0]
	v_pk_fma_f32 v[16:17], s[94:95], v[96:97], v[16:17] op_sel:[1,0,0]
	s_waitcnt lgkmcnt(0)
	s_load_dwordx8 s[64:71], s[20:21], 0x820
	s_load_dwordx8 s[72:79], s[20:21], 0xa20
	s_load_dwordx8 s[80:87], s[20:21], 0xc20
	s_load_dwordx8 s[88:95], s[20:21], 0xe20
	v_pk_fma_f32 v[18:19], s[32:33], v[34:35], v[18:19] op_sel_hi:[0,1,1]
	v_pk_fma_f32 v[20:21], s[32:33], v[36:37], v[20:21] op_sel_hi:[0,1,1]
	v_pk_fma_f32 v[22:23], s[40:41], v[34:35], v[22:23] op_sel_hi:[0,1,1]
	v_pk_fma_f32 v[24:25], s[40:41], v[36:37], v[24:25] op_sel_hi:[0,1,1]
	v_pk_fma_f32 v[26:27], s[48:49], v[34:35], v[26:27] op_sel_hi:[0,1,1]
	v_pk_fma_f32 v[28:29], s[48:49], v[36:37], v[28:29] op_sel_hi:[0,1,1]
	v_pk_fma_f32 v[30:31], s[56:57], v[34:35], v[30:31] op_sel_hi:[0,1,1]
	v_pk_fma_f32 v[32:33], s[56:57], v[36:37], v[32:33] op_sel_hi:[0,1,1]
	v_pk_fma_f32 v[18:19], s[32:33], v[38:39], v[18:19] op_sel:[1,0,0]
	v_pk_fma_f32 v[20:21], s[32:33], v[40:41], v[20:21] op_sel:[1,0,0]
	v_pk_fma_f32 v[22:23], s[40:41], v[38:39], v[22:23] op_sel:[1,0,0]
	v_pk_fma_f32 v[24:25], s[40:41], v[40:41], v[24:25] op_sel:[1,0,0]
	v_pk_fma_f32 v[26:27], s[48:49], v[38:39], v[26:27] op_sel:[1,0,0]
	v_pk_fma_f32 v[28:29], s[48:49], v[40:41], v[28:29] op_sel:[1,0,0]
	v_pk_fma_f32 v[30:31], s[56:57], v[38:39], v[30:31] op_sel:[1,0,0]
	v_pk_fma_f32 v[32:33], s[56:57], v[40:41], v[32:33] op_sel:[1,0,0]
	v_pk_fma_f32 v[18:19], s[34:35], v[42:43], v[18:19] op_sel_hi:[0,1,1]
	v_pk_fma_f32 v[20:21], s[34:35], v[44:45], v[20:21] op_sel_hi:[0,1,1]
	v_pk_fma_f32 v[22:23], s[42:43], v[42:43], v[22:23] op_sel_hi:[0,1,1]
	v_pk_fma_f32 v[24:25], s[42:43], v[44:45], v[24:25] op_sel_hi:[0,1,1]
	v_pk_fma_f32 v[26:27], s[50:51], v[42:43], v[26:27] op_sel_hi:[0,1,1]
	v_pk_fma_f32 v[28:29], s[50:51], v[44:45], v[28:29] op_sel_hi:[0,1,1]
	v_pk_fma_f32 v[30:31], s[58:59], v[42:43], v[30:31] op_sel_hi:[0,1,1]
	v_pk_fma_f32 v[32:33], s[58:59], v[44:45], v[32:33] op_sel_hi:[0,1,1]
	v_pk_fma_f32 v[18:19], s[34:35], v[46:47], v[18:19] op_sel:[1,0,0]
	v_pk_fma_f32 v[20:21], s[34:35], v[48:49], v[20:21] op_sel:[1,0,0]
	v_pk_fma_f32 v[22:23], s[42:43], v[46:47], v[22:23] op_sel:[1,0,0]
	v_pk_fma_f32 v[24:25], s[42:43], v[48:49], v[24:25] op_sel:[1,0,0]
	v_pk_fma_f32 v[26:27], s[50:51], v[46:47], v[26:27] op_sel:[1,0,0]
	v_pk_fma_f32 v[28:29], s[50:51], v[48:49], v[28:29] op_sel:[1,0,0]
	v_pk_fma_f32 v[30:31], s[58:59], v[46:47], v[30:31] op_sel:[1,0,0]
	v_pk_fma_f32 v[32:33], s[58:59], v[48:49], v[32:33] op_sel:[1,0,0]
	v_pk_fma_f32 v[18:19], s[36:37], v[50:51], v[18:19] op_sel_hi:[0,1,1]
	v_pk_fma_f32 v[20:21], s[36:37], v[52:53], v[20:21] op_sel_hi:[0,1,1]
	v_pk_fma_f32 v[22:23], s[44:45], v[50:51], v[22:23] op_sel_hi:[0,1,1]
	v_pk_fma_f32 v[24:25], s[44:45], v[52:53], v[24:25] op_sel_hi:[0,1,1]
	v_pk_fma_f32 v[26:27], s[52:53], v[50:51], v[26:27] op_sel_hi:[0,1,1]
	v_pk_fma_f32 v[28:29], s[52:53], v[52:53], v[28:29] op_sel_hi:[0,1,1]
	v_pk_fma_f32 v[30:31], s[60:61], v[50:51], v[30:31] op_sel_hi:[0,1,1]
	v_pk_fma_f32 v[32:33], s[60:61], v[52:53], v[32:33] op_sel_hi:[0,1,1]
	v_pk_fma_f32 v[18:19], s[36:37], v[54:55], v[18:19] op_sel:[1,0,0]
	v_pk_fma_f32 v[20:21], s[36:37], v[56:57], v[20:21] op_sel:[1,0,0]
	v_pk_fma_f32 v[22:23], s[44:45], v[54:55], v[22:23] op_sel:[1,0,0]
	v_pk_fma_f32 v[24:25], s[44:45], v[56:57], v[24:25] op_sel:[1,0,0]
	v_pk_fma_f32 v[26:27], s[52:53], v[54:55], v[26:27] op_sel:[1,0,0]
	v_pk_fma_f32 v[28:29], s[52:53], v[56:57], v[28:29] op_sel:[1,0,0]
	v_pk_fma_f32 v[30:31], s[60:61], v[54:55], v[30:31] op_sel:[1,0,0]
	v_pk_fma_f32 v[32:33], s[60:61], v[56:57], v[32:33] op_sel:[1,0,0]
	v_pk_fma_f32 v[18:19], s[38:39], v[58:59], v[18:19] op_sel_hi:[0,1,1]
	v_pk_fma_f32 v[20:21], s[38:39], v[60:61], v[20:21] op_sel_hi:[0,1,1]
	v_pk_fma_f32 v[22:23], s[46:47], v[58:59], v[22:23] op_sel_hi:[0,1,1]
	v_pk_fma_f32 v[24:25], s[46:47], v[60:61], v[24:25] op_sel_hi:[0,1,1]
	v_pk_fma_f32 v[26:27], s[54:55], v[58:59], v[26:27] op_sel_hi:[0,1,1]
	v_pk_fma_f32 v[28:29], s[54:55], v[60:61], v[28:29] op_sel_hi:[0,1,1]
	v_pk_fma_f32 v[30:31], s[62:63], v[58:59], v[30:31] op_sel_hi:[0,1,1]
	v_pk_fma_f32 v[32:33], s[62:63], v[60:61], v[32:33] op_sel_hi:[0,1,1]
	v_pk_fma_f32 v[18:19], s[38:39], v[62:63], v[18:19] op_sel:[1,0,0]
	v_pk_fma_f32 v[20:21], s[38:39], v[64:65], v[20:21] op_sel:[1,0,0]
	v_pk_fma_f32 v[22:23], s[46:47], v[62:63], v[22:23] op_sel:[1,0,0]
	v_pk_fma_f32 v[24:25], s[46:47], v[64:65], v[24:25] op_sel:[1,0,0]
	v_pk_fma_f32 v[26:27], s[54:55], v[62:63], v[26:27] op_sel:[1,0,0]
	v_pk_fma_f32 v[28:29], s[54:55], v[64:65], v[28:29] op_sel:[1,0,0]
	v_pk_fma_f32 v[30:31], s[62:63], v[62:63], v[30:31] op_sel:[1,0,0]
	v_pk_fma_f32 v[32:33], s[62:63], v[64:65], v[32:33] op_sel:[1,0,0]
	s_waitcnt lgkmcnt(0)
	v_pk_fma_f32 v[18:19], s[64:65], v[66:67], v[18:19] op_sel_hi:[0,1,1]
	v_pk_fma_f32 v[20:21], s[64:65], v[68:69], v[20:21] op_sel_hi:[0,1,1]
	v_pk_fma_f32 v[22:23], s[72:73], v[66:67], v[22:23] op_sel_hi:[0,1,1]
	v_pk_fma_f32 v[24:25], s[72:73], v[68:69], v[24:25] op_sel_hi:[0,1,1]
	v_pk_fma_f32 v[26:27], s[80:81], v[66:67], v[26:27] op_sel_hi:[0,1,1]
	v_pk_fma_f32 v[28:29], s[80:81], v[68:69], v[28:29] op_sel_hi:[0,1,1]
	v_pk_fma_f32 v[30:31], s[88:89], v[66:67], v[30:31] op_sel_hi:[0,1,1]
	v_pk_fma_f32 v[32:33], s[88:89], v[68:69], v[32:33] op_sel_hi:[0,1,1]
	v_pk_fma_f32 v[18:19], s[64:65], v[70:71], v[18:19] op_sel:[1,0,0]
	v_pk_fma_f32 v[20:21], s[64:65], v[72:73], v[20:21] op_sel:[1,0,0]
	v_pk_fma_f32 v[22:23], s[72:73], v[70:71], v[22:23] op_sel:[1,0,0]
	v_pk_fma_f32 v[24:25], s[72:73], v[72:73], v[24:25] op_sel:[1,0,0]
	v_pk_fma_f32 v[26:27], s[80:81], v[70:71], v[26:27] op_sel:[1,0,0]
	v_pk_fma_f32 v[28:29], s[80:81], v[72:73], v[28:29] op_sel:[1,0,0]
	v_pk_fma_f32 v[30:31], s[88:89], v[70:71], v[30:31] op_sel:[1,0,0]
	v_pk_fma_f32 v[32:33], s[88:89], v[72:73], v[32:33] op_sel:[1,0,0]
	v_pk_fma_f32 v[18:19], s[66:67], v[74:75], v[18:19] op_sel_hi:[0,1,1]
	v_pk_fma_f32 v[20:21], s[66:67], v[76:77], v[20:21] op_sel_hi:[0,1,1]
	v_pk_fma_f32 v[22:23], s[74:75], v[74:75], v[22:23] op_sel_hi:[0,1,1]
	v_pk_fma_f32 v[24:25], s[74:75], v[76:77], v[24:25] op_sel_hi:[0,1,1]
	v_pk_fma_f32 v[26:27], s[82:83], v[74:75], v[26:27] op_sel_hi:[0,1,1]
	v_pk_fma_f32 v[28:29], s[82:83], v[76:77], v[28:29] op_sel_hi:[0,1,1]
	v_pk_fma_f32 v[30:31], s[90:91], v[74:75], v[30:31] op_sel_hi:[0,1,1]
	v_pk_fma_f32 v[32:33], s[90:91], v[76:77], v[32:33] op_sel_hi:[0,1,1]
	v_pk_fma_f32 v[18:19], s[66:67], v[78:79], v[18:19] op_sel:[1,0,0]
	v_pk_fma_f32 v[20:21], s[66:67], v[80:81], v[20:21] op_sel:[1,0,0]
	v_pk_fma_f32 v[22:23], s[74:75], v[78:79], v[22:23] op_sel:[1,0,0]
	v_pk_fma_f32 v[24:25], s[74:75], v[80:81], v[24:25] op_sel:[1,0,0]
	v_pk_fma_f32 v[26:27], s[82:83], v[78:79], v[26:27] op_sel:[1,0,0]
	v_pk_fma_f32 v[28:29], s[82:83], v[80:81], v[28:29] op_sel:[1,0,0]
	v_pk_fma_f32 v[30:31], s[90:91], v[78:79], v[30:31] op_sel:[1,0,0]
	v_pk_fma_f32 v[32:33], s[90:91], v[80:81], v[32:33] op_sel:[1,0,0]
	v_pk_fma_f32 v[18:19], s[68:69], v[82:83], v[18:19] op_sel_hi:[0,1,1]
	v_pk_fma_f32 v[20:21], s[68:69], v[84:85], v[20:21] op_sel_hi:[0,1,1]
	v_pk_fma_f32 v[22:23], s[76:77], v[82:83], v[22:23] op_sel_hi:[0,1,1]
	v_pk_fma_f32 v[24:25], s[76:77], v[84:85], v[24:25] op_sel_hi:[0,1,1]
	v_pk_fma_f32 v[26:27], s[84:85], v[82:83], v[26:27] op_sel_hi:[0,1,1]
	v_pk_fma_f32 v[28:29], s[84:85], v[84:85], v[28:29] op_sel_hi:[0,1,1]
	v_pk_fma_f32 v[30:31], s[92:93], v[82:83], v[30:31] op_sel_hi:[0,1,1]
	v_pk_fma_f32 v[32:33], s[92:93], v[84:85], v[32:33] op_sel_hi:[0,1,1]
	v_pk_fma_f32 v[18:19], s[68:69], v[86:87], v[18:19] op_sel:[1,0,0]
	v_pk_fma_f32 v[20:21], s[68:69], v[88:89], v[20:21] op_sel:[1,0,0]
	v_pk_fma_f32 v[22:23], s[76:77], v[86:87], v[22:23] op_sel:[1,0,0]
	v_pk_fma_f32 v[24:25], s[76:77], v[88:89], v[24:25] op_sel:[1,0,0]
	v_pk_fma_f32 v[26:27], s[84:85], v[86:87], v[26:27] op_sel:[1,0,0]
	v_pk_fma_f32 v[28:29], s[84:85], v[88:89], v[28:29] op_sel:[1,0,0]
	v_pk_fma_f32 v[30:31], s[92:93], v[86:87], v[30:31] op_sel:[1,0,0]
	v_pk_fma_f32 v[32:33], s[92:93], v[88:89], v[32:33] op_sel:[1,0,0]
	v_pk_fma_f32 v[18:19], s[70:71], v[90:91], v[18:19] op_sel_hi:[0,1,1]
	v_pk_fma_f32 v[20:21], s[70:71], v[92:93], v[20:21] op_sel_hi:[0,1,1]
	v_pk_fma_f32 v[22:23], s[78:79], v[90:91], v[22:23] op_sel_hi:[0,1,1]
	v_pk_fma_f32 v[24:25], s[78:79], v[92:93], v[24:25] op_sel_hi:[0,1,1]
	v_pk_fma_f32 v[26:27], s[86:87], v[90:91], v[26:27] op_sel_hi:[0,1,1]
	v_pk_fma_f32 v[28:29], s[86:87], v[92:93], v[28:29] op_sel_hi:[0,1,1]
	v_pk_fma_f32 v[30:31], s[94:95], v[90:91], v[30:31] op_sel_hi:[0,1,1]
	v_pk_fma_f32 v[32:33], s[94:95], v[92:93], v[32:33] op_sel_hi:[0,1,1]
	v_pk_fma_f32 v[18:19], s[70:71], v[94:95], v[18:19] op_sel:[1,0,0]
	v_pk_fma_f32 v[20:21], s[70:71], v[96:97], v[20:21] op_sel:[1,0,0]
	v_pk_fma_f32 v[22:23], s[78:79], v[94:95], v[22:23] op_sel:[1,0,0]
	v_pk_fma_f32 v[24:25], s[78:79], v[96:97], v[24:25] op_sel:[1,0,0]
	v_pk_fma_f32 v[26:27], s[86:87], v[94:95], v[26:27] op_sel:[1,0,0]
	v_pk_fma_f32 v[28:29], s[86:87], v[96:97], v[28:29] op_sel:[1,0,0]
	v_pk_fma_f32 v[30:31], s[94:95], v[94:95], v[30:31] op_sel:[1,0,0]
	v_pk_fma_f32 v[32:33], s[94:95], v[96:97], v[32:33] op_sel:[1,0,0]
	s_lshl_b32 s9, s23, 13
	v_add_u32_e32 v98, s9, v100
	ds_write_b128 v98, v[2:5] offset:0
	ds_write_b128 v98, v[6:9] offset:1024
	ds_write_b128 v98, v[10:13] offset:2048
	ds_write_b128 v98, v[14:17] offset:3072
	ds_write_b128 v98, v[18:21] offset:4096
	ds_write_b128 v98, v[22:25] offset:5120
	ds_write_b128 v98, v[26:29] offset:6144
	ds_write_b128 v98, v[30:33] offset:7168
	s_lshl_b32 s9, s23, 10
	v_add_u32_e32 v99, s9, v100
	s_waitcnt lgkmcnt(0)
	s_barrier
	ds_read_b128 v[34:37], v99 offset:0
	ds_read_b128 v[38:41], v99 offset:8192
	ds_read_b128 v[42:45], v99 offset:16384
	ds_read_b128 v[46:49], v99 offset:24576
	ds_read_b128 v[50:53], v99 offset:32768
	ds_read_b128 v[54:57], v99 offset:40960
	ds_read_b128 v[58:61], v99 offset:49152
	ds_read_b128 v[62:65], v99 offset:57344
	s_lshl_b32 s8, s27, 3
	s_add_u32 s8, s8, s23
	s_lshl_b32 s8, s8, 11
	s_lshl_b32 s9, s30, 10
	s_add_u32 s8, s8, s9
	s_add_u32 s28, s28, s8
	s_addc_u32 s29, s29, 0
	s_waitcnt lgkmcnt(6)
	v_pk_add_f32 v[34:35], v[34:35], v[38:39]
	v_pk_add_f32 v[36:37], v[36:37], v[40:41]
	s_waitcnt lgkmcnt(5)
	v_pk_add_f32 v[34:35], v[34:35], v[42:43]
	v_pk_add_f32 v[36:37], v[36:37], v[44:45]
	s_waitcnt lgkmcnt(4)
	v_pk_add_f32 v[34:35], v[34:35], v[46:47]
	v_pk_add_f32 v[36:37], v[36:37], v[48:49]
	s_waitcnt lgkmcnt(3)
	v_pk_add_f32 v[34:35], v[34:35], v[50:51]
	v_pk_add_f32 v[36:37], v[36:37], v[52:53]
	s_waitcnt lgkmcnt(2)
	v_pk_add_f32 v[34:35], v[34:35], v[54:55]
	v_pk_add_f32 v[36:37], v[36:37], v[56:57]
	s_waitcnt lgkmcnt(1)
	v_pk_add_f32 v[34:35], v[34:35], v[58:59]
	v_pk_add_f32 v[36:37], v[36:37], v[60:61]
	s_waitcnt lgkmcnt(0)
	v_pk_add_f32 v[34:35], v[34:35], v[62:63]
	v_pk_add_f32 v[36:37], v[36:37], v[64:65]
	global_store_dwordx4 v100, v[34:37], s[28:29]

	.amdhsa_kernel _Z11prep_kernelPKfS0_S0_PDF16_PfPiS0_S1_
		.amdhsa_group_segment_fixed_size 65536
		.amdhsa_private_segment_fixed_size 0
		.amdhsa_kernarg_size 64
		.amdhsa_user_sgpr_count 2
		.amdhsa_user_sgpr_dispatch_ptr 0
		.amdhsa_user_sgpr_queue_ptr 0
		.amdhsa_user_sgpr_kernarg_segment_ptr 1
		.amdhsa_user_sgpr_dispatch_id 0
		.amdhsa_user_sgpr_kernarg_preload_length 0
		.amdhsa_user_sgpr_kernarg_preload_offset 0
		.amdhsa_user_sgpr_private_segment_size 0
		.amdhsa_uses_dynamic_stack 0
		.amdhsa_enable_private_segment 0
		.amdhsa_system_sgpr_workgroup_id_x 1
		.amdhsa_system_sgpr_workgroup_id_y 0
		.amdhsa_system_sgpr_workgroup_id_z 0
		.amdhsa_system_sgpr_workgroup_info 0
		.amdhsa_system_vgpr_workitem_id 0
		.amdhsa_next_free_vgpr 160
		.amdhsa_next_free_sgpr 96
		.amdhsa_accum_offset 160
		.amdhsa_reserve_vcc 1
		.amdhsa_float_round_mode_32 0
		.amdhsa_float_round_mode_16_64 0
		.amdhsa_float_denorm_mode_32 3
		.amdhsa_float_denorm_mode_16_64 3
		.amdhsa_dx10_clamp 1
		.amdhsa_ieee_mode 1
		.amdhsa_fp16_overflow 0
		.amdhsa_tg_split 0
		.amdhsa_exception_fp_ieee_invalid_op 0
		.amdhsa_exception_fp_denorm_src 0
		.amdhsa_exception_fp_ieee_div_zero 0
		.amdhsa_exception_fp_ieee_overflow 0
		.amdhsa_exception_fp_ieee_underflow 0
		.amdhsa_exception_fp_ieee_inexact 0
		.amdhsa_exception_int_div_zero 0
	.end_amdhsa_kernel

amdhsa.kernels:
  - .agpr_count:     0
    .args:
      - .actual_access:  read_only
        .address_space:  global
        .offset:         0
        .size:           8
        .value_kind:     global_buffer
      - .actual_access:  read_only
        .address_space:  global
        .offset:         8
        .size:           8
        .value_kind:     global_buffer
      - .actual_access:  read_only
        .address_space:  global
        .offset:         16
        .size:           8
        .value_kind:     global_buffer
      - .actual_access:  write_only
        .address_space:  global
        .offset:         24
        .size:           8
        .value_kind:     global_buffer
      - .actual_access:  write_only
        .address_space:  global
        .offset:         32
        .size:           8
        .value_kind:     global_buffer
      - .actual_access:  write_only
        .address_space:  global
        .offset:         40
        .size:           8
        .value_kind:     global_buffer
      - .actual_access:  read_only
        .address_space:  global
        .offset:         48
        .size:           8
        .value_kind:     global_buffer
      - .actual_access:  write_only
        .address_space:  global
        .offset:         56
        .size:           8
        .value_kind:     global_buffer
    .group_segment_fixed_size: 65536
    .kernarg_segment_align: 8
    .kernarg_segment_size: 64
    .language:       OpenCL C
    .language_version:
      - 2
      - 0
    .max_flat_workgroup_size: 512
    .name:           _Z11prep_kernelPKfS0_S0_PDF16_PfPiS0_S1_
    .private_segment_fixed_size: 0
    .sgpr_count:     102
    .sgpr_spill_count: 0
    .symbol:         _Z11prep_kernelPKfS0_S0_PDF16_PfPiS0_S1_.kd
    .uniform_work_group_size: 1
    .uses_dynamic_stack: false
    .vgpr_count:     160
    .vgpr_spill_count: 0
    .wavefront_size: 64
  - .agpr_count:     256
    .args:
      - .actual_access:  read_only
        .address_space:  global
        .offset:         0
        .size:           8
        .value_kind:     global_buffer
      - .actual_access:  read_only
        .address_space:  global
        .offset:         8
        .size:           8
        .value_kind:     global_buffer
      - .actual_access:  read_only
        .address_space:  global
        .offset:         16
        .size:           8
        .value_kind:     global_buffer
      - .actual_access:  write_only
        .address_space:  global
        .offset:         24
        .size:           8
        .value_kind:     global_buffer
      - .actual_access:  read_only
        .address_space:  global
        .offset:         32
        .size:           8
        .value_kind:     global_buffer
    .group_segment_fixed_size: 148624
    .kernarg_segment_align: 8
    .kernarg_segment_size: 40
    .language:       OpenCL C
    .language_version:
      - 2
      - 0
    .max_flat_workgroup_size: 256
    .name:           _Z10ode_kernelPKfPKDF16_S2_PfPKi
    .private_segment_fixed_size: 0
    .sgpr_count:     59
    .sgpr_spill_count: 0
    .symbol:         _Z10ode_kernelPKfPKDF16_S2_PfPKi.kd
    .uniform_work_group_size: 1
    .uses_dynamic_stack: false
    .vgpr_count:     512
    .vgpr_spill_count: 0
    .wavefront_size: 64
